# rwkv_pre S3 diagonal-block solve rewritten by hand: right-looking update order with independent row-pair chains (same per-row FMA order), own coefficient register layout
# speedup vs baseline: 1.0092x; 1.0092x over previous
.LBB0_623:
	v_fmac_f32_e32 v3, v228, v2
	s_nop 1
	v_pk_fma_f32 v[4:5], v[70:71], v[2:3], v[4:5] op_sel_hi:[1,0,1]
	v_pk_fma_f32 v[6:7], v[72:73], v[2:3], v[6:7] op_sel_hi:[1,0,1]
	v_pk_fma_f32 v[8:9], v[74:75], v[2:3], v[8:9] op_sel_hi:[1,0,1]
	v_pk_fma_f32 v[10:11], v[76:77], v[2:3], v[10:11] op_sel_hi:[1,0,1]
	v_pk_fma_f32 v[12:13], v[78:79], v[2:3], v[12:13] op_sel_hi:[1,0,1]
	v_pk_fma_f32 v[14:15], v[80:81], v[2:3], v[14:15] op_sel_hi:[1,0,1]
	v_pk_fma_f32 v[16:17], v[82:83], v[2:3], v[16:17] op_sel_hi:[1,0,1]
	v_pk_fma_f32 v[4:5], v[84:85], v[2:3], v[4:5] op_sel:[0,1,0]
	v_pk_fma_f32 v[6:7], v[86:87], v[2:3], v[6:7] op_sel:[0,1,0]
	v_pk_fma_f32 v[8:9], v[88:89], v[2:3], v[8:9] op_sel:[0,1,0]
	v_pk_fma_f32 v[10:11], v[90:91], v[2:3], v[10:11] op_sel:[0,1,0]
	v_pk_fma_f32 v[12:13], v[92:93], v[2:3], v[12:13] op_sel:[0,1,0]
	v_pk_fma_f32 v[14:15], v[94:95], v[2:3], v[14:15] op_sel:[0,1,0]
	v_pk_fma_f32 v[16:17], v[96:97], v[2:3], v[16:17] op_sel:[0,1,0]
	v_fmac_f32_e32 v5, v230, v4
	s_nop 1
	v_pk_fma_f32 v[6:7], v[98:99], v[4:5], v[6:7] op_sel_hi:[1,0,1]
	v_pk_fma_f32 v[8:9], v[100:101], v[4:5], v[8:9] op_sel_hi:[1,0,1]
	v_pk_fma_f32 v[10:11], v[102:103], v[4:5], v[10:11] op_sel_hi:[1,0,1]
	v_pk_fma_f32 v[12:13], v[104:105], v[4:5], v[12:13] op_sel_hi:[1,0,1]
	v_pk_fma_f32 v[14:15], v[106:107], v[4:5], v[14:15] op_sel_hi:[1,0,1]
	v_pk_fma_f32 v[16:17], v[108:109], v[4:5], v[16:17] op_sel_hi:[1,0,1]
	v_pk_fma_f32 v[6:7], v[110:111], v[4:5], v[6:7] op_sel:[0,1,0]
	v_pk_fma_f32 v[8:9], v[112:113], v[4:5], v[8:9] op_sel:[0,1,0]
	v_pk_fma_f32 v[10:11], v[114:115], v[4:5], v[10:11] op_sel:[0,1,0]
	v_pk_fma_f32 v[12:13], v[116:117], v[4:5], v[12:13] op_sel:[0,1,0]
	v_pk_fma_f32 v[14:15], v[118:119], v[4:5], v[14:15] op_sel:[0,1,0]
	v_pk_fma_f32 v[16:17], v[120:121], v[4:5], v[16:17] op_sel:[0,1,0]
	v_fmac_f32_e32 v7, v233, v6
	s_nop 1
	v_pk_fma_f32 v[8:9], v[122:123], v[6:7], v[8:9] op_sel_hi:[1,0,1]
	v_pk_fma_f32 v[10:11], v[124:125], v[6:7], v[10:11] op_sel_hi:[1,0,1]
	v_pk_fma_f32 v[12:13], v[126:127], v[6:7], v[12:13] op_sel_hi:[1,0,1]
	v_pk_fma_f32 v[14:15], v[128:129], v[6:7], v[14:15] op_sel_hi:[1,0,1]
	v_pk_fma_f32 v[16:17], v[130:131], v[6:7], v[16:17] op_sel_hi:[1,0,1]
	v_pk_fma_f32 v[8:9], v[132:133], v[6:7], v[8:9] op_sel:[0,1,0]
	v_pk_fma_f32 v[10:11], v[134:135], v[6:7], v[10:11] op_sel:[0,1,0]
	v_pk_fma_f32 v[12:13], v[136:137], v[6:7], v[12:13] op_sel:[0,1,0]
	v_pk_fma_f32 v[14:15], v[138:139], v[6:7], v[14:15] op_sel:[0,1,0]
	v_pk_fma_f32 v[16:17], v[140:141], v[6:7], v[16:17] op_sel:[0,1,0]
	v_fmac_f32_e32 v9, v235, v8
	s_nop 1
	v_pk_fma_f32 v[10:11], v[142:143], v[8:9], v[10:11] op_sel_hi:[1,0,1]
	v_pk_fma_f32 v[12:13], v[144:145], v[8:9], v[12:13] op_sel_hi:[1,0,1]
	v_pk_fma_f32 v[14:15], v[146:147], v[8:9], v[14:15] op_sel_hi:[1,0,1]
	v_pk_fma_f32 v[16:17], v[148:149], v[8:9], v[16:17] op_sel_hi:[1,0,1]
	v_pk_fma_f32 v[10:11], v[150:151], v[8:9], v[10:11] op_sel:[0,1,0]
	v_pk_fma_f32 v[12:13], v[152:153], v[8:9], v[12:13] op_sel:[0,1,0]
	v_pk_fma_f32 v[14:15], v[154:155], v[8:9], v[14:15] op_sel:[0,1,0]
	v_pk_fma_f32 v[16:17], v[156:157], v[8:9], v[16:17] op_sel:[0,1,0]
	v_fmac_f32_e32 v11, v236, v10
	s_nop 1
	v_pk_fma_f32 v[12:13], v[158:159], v[10:11], v[12:13] op_sel_hi:[1,0,1]
	v_pk_fma_f32 v[14:15], v[160:161], v[10:11], v[14:15] op_sel_hi:[1,0,1]
	v_pk_fma_f32 v[16:17], v[162:163], v[10:11], v[16:17] op_sel_hi:[1,0,1]
	v_pk_fma_f32 v[12:13], v[164:165], v[10:11], v[12:13] op_sel:[0,1,0]
	v_pk_fma_f32 v[14:15], v[188:189], v[10:11], v[14:15] op_sel:[0,1,0]
	v_pk_fma_f32 v[16:17], v[190:191], v[10:11], v[16:17] op_sel:[0,1,0]
	v_fmac_f32_e32 v13, v237, v12
	s_nop 1
	v_pk_fma_f32 v[14:15], v[192:193], v[12:13], v[14:15] op_sel_hi:[1,0,1]
	v_pk_fma_f32 v[16:17], v[194:195], v[12:13], v[16:17] op_sel_hi:[1,0,1]
	v_pk_fma_f32 v[14:15], v[196:197], v[12:13], v[14:15] op_sel:[0,1,0]
	v_pk_fma_f32 v[16:17], v[198:199], v[12:13], v[16:17] op_sel:[0,1,0]
	v_fmac_f32_e32 v15, v238, v14
	s_nop 1
	v_pk_fma_f32 v[16:17], v[200:201], v[14:15], v[16:17] op_sel_hi:[1,0,1]
	s_nop 1
	v_pk_fma_f32 v[16:17], v[202:203], v[14:15], v[16:17] op_sel:[0,1,0]
	s_nop 1
	v_fmac_f32_e32 v17, v239, v16
	s_nop 0
	v_cvt_pk_bf16_f32 v18, v2, v3
	v_cvt_pk_bf16_f32 v19, v4, v5
	v_cvt_pk_bf16_f32 v20, v6, v7
	v_cvt_pk_bf16_f32 v21, v8, v9
	v_cvt_pk_bf16_f32 v22, v10, v11
	v_cvt_pk_bf16_f32 v23, v12, v13
	v_cvt_pk_bf16_f32 v24, v14, v15
	v_cvt_pk_bf16_f32 v25, v16, v17
	ds_write_b128 v169, v[18:21]
	ds_write_b128 v169, v[22:25] offset:16

.LBB0_634:
	s_or_b64 exec, exec, s[14:15]
	s_add_i32 s14, s11, 0
	s_add_i32 s15, s14, 0x1d400
	v_mov_b32_e32 v18, s15
	ds_read_b32 v228, v18 offset:4
	ds_read_b64 v[70:71], v18 offset:8
	ds_read_b128 v[72:75], v18 offset:16
	ds_read_b128 v[76:79], v18 offset:32
	ds_read_b128 v[80:83], v18 offset:48
	ds_read_b64 v[84:85], v18 offset:264
	ds_read_b128 v[86:89], v18 offset:272
	ds_read_b128 v[90:93], v18 offset:288
	ds_read_b128 v[94:97], v18 offset:304
	ds_read_b32 v230, v18 offset:524
	ds_read_b128 v[98:101], v18 offset:528
	ds_read_b128 v[102:105], v18 offset:544
	ds_read_b128 v[106:109], v18 offset:560
	ds_read_b128 v[110:113], v18 offset:784
	ds_read_b128 v[114:117], v18 offset:800
	ds_read_b128 v[118:121], v18 offset:816
	ds_read_b32 v233, v18 offset:1044
	ds_read_b64 v[122:123], v18 offset:1048
	ds_read_b128 v[124:127], v18 offset:1056
	ds_read_b128 v[128:131], v18 offset:1072
	ds_read_b64 v[132:133], v18 offset:1304
	ds_read_b128 v[134:137], v18 offset:1312
	ds_read_b128 v[138:141], v18 offset:1328
	ds_read_b32 v235, v18 offset:1564
	ds_read_b128 v[142:145], v18 offset:1568
	ds_read_b128 v[146:149], v18 offset:1584
	ds_read_b128 v[150:153], v18 offset:1824
	ds_read_b128 v[154:157], v18 offset:1840
	ds_read_b32 v236, v18 offset:2084
	ds_read_b64 v[158:159], v18 offset:2088
	ds_read_b128 v[160:163], v18 offset:2096
	ds_read_b64 v[164:165], v18 offset:2344
	ds_read_b128 v[188:191], v18 offset:2352
	ds_read_b32 v237, v18 offset:2604
	ds_read_b128 v[192:195], v18 offset:2608
	ds_read_b128 v[196:199], v18 offset:2864
	ds_read_b32 v238, v18 offset:3124
	ds_read_b64 v[200:201], v18 offset:3128
	ds_read_b64 v[202:203], v18 offset:3384
	ds_read_b32 v239, v18 offset:3644
